# lean attention loop + V-tile loads through a running SGPR pointer with immediate offsets and a 3-instruction loop test (12 fewer SALU per iteration)
# speedup vs baseline: 1.0046x; 1.0046x over previous
.LBB0_733:
	s_or_b64 exec, exec, s[8:9]
	s_movk_i32 s4, 0xf0
	s_cmp_lg_u32 0, -1
	v_lshlrev_b32_e32 v39, 8, v141
	v_bitop3_b32 v80, v142, s4, v136 bitop3:0x48
	s_cselect_b32 s10, 0, 0
	v_cvt_pk_bf16_f32 v96, v134, v135
	v_cvt_pk_bf16_f32 v97, v132, v133
	v_cvt_pk_bf16_f32 v98, v130, v131
	v_cvt_pk_bf16_f32 v99, v128, v129
	v_cvt_pk_bf16_f32 v100, v126, v127
	v_cvt_pk_bf16_f32 v101, v124, v125
	v_cvt_pk_bf16_f32 v102, v122, v123
	v_cvt_pk_bf16_f32 v103, v120, v121
	v_cvt_pk_bf16_f32 v104, v70, v71
	v_cvt_pk_bf16_f32 v105, v74, v75
	v_cvt_pk_bf16_f32 v106, v64, v65
	v_cvt_pk_bf16_f32 v107, v68, v69
	v_cvt_pk_bf16_f32 v108, v60, v61
	v_cvt_pk_bf16_f32 v109, v66, v67
	v_cvt_pk_bf16_f32 v110, v56, v57
	v_cvt_pk_bf16_f32 v111, v58, v59
	v_cvt_pk_bf16_f32 v112, v112, v113
	v_cvt_pk_bf16_f32 v113, v118, v119
	v_cvt_pk_bf16_f32 v114, v114, v115
	v_cvt_pk_bf16_f32 v115, v116, v117
	v_cvt_pk_bf16_f32 v116, v78, v79
	v_cvt_pk_bf16_f32 v117, v76, v77
	v_cvt_pk_bf16_f32 v118, v72, v73
	v_cvt_pk_bf16_f32 v119, v62, v63
	v_cvt_pk_bf16_f32 v120, v52, v53
	v_cvt_pk_bf16_f32 v121, v54, v55
	v_cvt_pk_bf16_f32 v122, v46, v47
	v_cvt_pk_bf16_f32 v123, v50, v51
	v_cvt_pk_bf16_f32 v124, v44, v45
	v_cvt_pk_bf16_f32 v125, v48, v49
	v_cvt_pk_bf16_f32 v126, v40, v41
	v_cvt_pk_bf16_f32 v127, v42, v43
	v_readlane_b32 s100, v250, 8
	v_mbcnt_lo_u32_b32 v68, -1, 0
	v_mbcnt_hi_u32_b32 v68, -1, v68
	s_nop 1
	v_add_u32_e32 v69, s100, v68
	v_lshrrev_b32_e32 v70, 3, v69
	v_and_b32_e32 v71, 7, v69
	v_lshrrev_b32_e32 v72, 2, v71
	v_bfe_u32 v73, v71, 1, 1
	v_and_b32_e32 v74, 1, v71
	v_lshlrev_b32_e32 v74, 1, v74
	v_lshl_add_u32 v75, v72, 2, v74
	v_bfe_u32 v76, v70, 1, 3
	v_xor_b32_e32 v77, v75, v76
	v_add_u32_e32 v78, 1, v75
	v_xor_b32_e32 v78, v78, v76
	v_lshlrev_b32_e32 v79, 7, v70
	v_lshl_add_u32 v79, v73, 3, v79
	v_lshl_add_u32 v64, v77, 4, v79
	v_lshl_add_u32 v65, v78, 4, v79
	v_add_u32_e32 v66, 0x2000, v64
	v_add_u32_e32 v67, 0x2000, v65
	v_or_b32_e32 v81, v39, v80
	s_add_i32 s15, s10, 0x10000
	v_and_b32_e32 v82, 6, v137
	v_lshrrev_b32_e32 v84, 4, v136
	s_waitcnt vmcnt(0)
	s_waitcnt vmcnt(0)
	s_add_i32 s11, s10, 0x12000
	v_lshl_add_u32 v83, v139, 7, s10
	v_bitop3_b32 v85, v84, v82, 7 bitop3:0x6c
	v_and_b32_e32 v86, 8, v138
	v_or_b32_e32 v82, 1, v82
	v_add_u32_e32 v225, s15, v81
	s_waitcnt vmcnt(4)
	ds_write_b128 v225, v[24:27] offset:0
	v_lshlrev_b32_e32 v85, 4, v85
	v_add_u32_e32 v87, v83, v86
	v_bitop3_b32 v82, v84, v82, 7 bitop3:0x6c
	v_add3_u32 v226, v80, s11, v39
	ds_write_b128 v226, v[28:31] offset:0
	v_lshlrev_b32_e32 v82, 4, v82
	v_add_u32_e32 v227, v87, v85
	ds_write_b64 v64, v[12:13] offset:0
	v_lshrrev_b32_e32 v32, 5, v136
	v_add_u32_e32 v83, 0x2000, v83
	v_or_b32_e32 v84, v85, v86
	v_add_u32_e32 v228, v87, v82
	ds_write_b64 v65, v[14:15] offset:0
	v_xor_b32_e32 v32, v32, v137
	v_or_b32_e32 v86, v82, v86
	v_add_u32_e32 v229, v84, v83
	ds_write_b64 v66, v[4:5] offset:0
	v_lshlrev_b32_e32 v32, 4, v32
	v_add_u32_e32 v184, v86, v83
	ds_write_b64 v67, v[6:7] offset:0
	v_lshlrev_b32_e32 v33, 8, v143
	v_and_b32_e32 v32, 16, v32
	v_bfe_u32 v35, v137, 1, 3
	s_waitcnt vmcnt(4)
	ds_write_b128 v225, v[20:23] offset:0x4000
	v_lshlrev_b32_e32 v36, 5, v35
	v_add3_u32 v32, v33, s15, v32
	s_movk_i32 s16, 0x60
	ds_write_b128 v226, v[16:19] offset:0x4000
	v_xad_u32 v204, v36, s16, v32
	s_movk_i32 s16, 0x80
	ds_write_b64 v64, v[8:9] offset:0x4000
	v_xad_u32 v205, v36, s16, v32
	s_movk_i32 s16, 0xa0
	ds_write_b64 v65, v[10:11] offset:0x4000
	s_add_u32 s8, s6, 0x100
	v_xad_u32 v206, v36, s16, v32
	s_movk_i32 s16, 0xc0
	ds_write_b64 v66, v[0:1] offset:0x4000
	s_addc_u32 s9, s7, 0
	v_xad_u32 v207, v36, s16, v32
	s_movk_i32 s16, 0xe0
	ds_write_b64 v67, v[2:3] offset:0x4000
	v_add_u32_e32 v201, v32, v36
	v_xad_u32 v202, v36, 32, v32
	v_xad_u32 v203, v36, 64, v32
	v_xad_u32 v208, v36, s16, v32
	v_lshl_add_u32 v32, v143, 7, s10
	s_add_u32 s10, s78, 0x20000
	global_load_dwordx4 v[132:135], v198, s[8:9]
	s_addc_u32 s11, s79, 0
	global_load_dwordx4 v[128:131], v199, s[8:9]
	v_lshrrev_b32_e32 v34, 1, v137
	global_load_dwordx4 v[136:139], v196, s[10:11]
	s_add_u32 s6, s6, 0x180
	v_bitop3_b32 v34, v140, v34, 7 bitop3:0x78
	v_bitop3_b32 v37, v140, v35, 2 bitop3:0x36
	v_bitop3_b32 v38, v140, v35, 4 bitop3:0x36
	v_bitop3_b32 v35, v140, v35, 6 bitop3:0x36
	global_load_dwordx4 v[140:143], v197, s[10:11]
	s_addc_u32 s7, s7, 0
	s_add_u32 s8, s78, 0x30000
	global_load_dwordx4 v[148:151], v198, s[6:7]
	s_addc_u32 s9, s79, 0
	global_load_dwordx4 v[144:147], v199, s[6:7]
	global_load_dwordx4 v[152:155], v196, s[8:9]
	s_add_u32 s10, s13, s14
	global_load_dwordx4 v[156:159], v197, s[8:9]
	s_addc_u32 s11, s12, 0
	s_add_u32 s12, s41, s30
	v_mov_b32_e32 v0, 0
	s_mov_b32 s4, 0
	v_lshl_add_u32 v209, v34, 4, v32
	v_lshl_add_u32 v210, v37, 4, v32
	v_lshl_add_u32 v211, v38, 4, v32
	v_lshl_add_u32 v224, v35, 4, v32
	s_addc_u32 s13, 0, s31
	v_mov_b32_e32 v1, v0
	v_mov_b32_e32 v2, v0
	v_mov_b32_e32 v3, v0
	v_mov_b32_e32 v4, v0
	v_mov_b32_e32 v5, v0
	v_mov_b32_e32 v6, v0
	v_mov_b32_e32 v7, v0
	v_mov_b32_e32 v8, v0
	v_mov_b32_e32 v9, v0
	v_mov_b32_e32 v10, v0
	v_mov_b32_e32 v11, v0
	v_mov_b32_e32 v12, v0
	v_mov_b32_e32 v13, v0
	v_mov_b32_e32 v14, v0
	v_mov_b32_e32 v15, v0
	v_mov_b32_e32 v16, v0
	v_mov_b32_e32 v17, v0
	v_mov_b32_e32 v18, v0
	v_mov_b32_e32 v19, v0
	v_mov_b32_e32 v20, v0
	v_mov_b32_e32 v21, v0
	v_mov_b32_e32 v22, v0
	v_mov_b32_e32 v23, v0
	v_mov_b32_e32 v24, v0
	v_mov_b32_e32 v25, v0
	v_mov_b32_e32 v26, v0
	v_mov_b32_e32 v27, v0
	v_mov_b32_e32 v28, v0
	v_mov_b32_e32 v29, v0
	v_mov_b32_e32 v30, v0
	v_mov_b32_e32 v31, v0
	v_mov_b32_e32 v32, v0
	v_mov_b32_e32 v33, v0
	v_mov_b32_e32 v34, v0
	v_mov_b32_e32 v35, v0
	v_mov_b32_e32 v36, v0
	v_mov_b32_e32 v37, v0
	v_mov_b32_e32 v38, v0
	v_mov_b32_e32 v39, v0
	v_mov_b32_e32 v40, v0
	v_mov_b32_e32 v41, v0
	v_mov_b32_e32 v42, v0
	v_mov_b32_e32 v43, v0
	v_mov_b32_e32 v44, v0
	v_mov_b32_e32 v45, v0
	v_mov_b32_e32 v46, v0
	v_mov_b32_e32 v47, v0
	v_mov_b32_e32 v48, v0
	v_mov_b32_e32 v49, v0
	v_mov_b32_e32 v50, v0
	v_mov_b32_e32 v51, v0
	v_mov_b32_e32 v52, v0
	v_mov_b32_e32 v53, v0
	v_mov_b32_e32 v54, v0
	v_mov_b32_e32 v55, v0
	v_mov_b32_e32 v56, v0
	v_mov_b32_e32 v57, v0
	v_mov_b32_e32 v58, v0
	v_mov_b32_e32 v59, v0
	v_mov_b32_e32 v60, v0
	v_mov_b32_e32 v61, v0
	v_mov_b32_e32 v62, v0
	v_mov_b32_e32 v63, v0
	v_mov_b32_e32 v160, v0
	v_mov_b32_e32 v161, v0
	v_mov_b32_e32 v227, v64
	v_mov_b32_e32 v228, v65
	v_mov_b32_e32 v229, v66
	v_mov_b32_e32 v184, v67
	v_readlane_b32 s100, v250, 8
	v_mbcnt_lo_u32_b32 v68, -1, 0
	v_mbcnt_hi_u32_b32 v68, -1, v68
	v_and_b32_e32 v69, 15, v68
	v_lshrrev_b32_e32 v70, 4, v68
	v_lshlrev_b32_e32 v72, 8, v69
	v_add_u32_e32 v72, 0x10000, v72
	v_add_u32_e32 v71, 0, v70
	v_xor_b32_e32 v71, v71, v69
	v_lshl_add_u32 v201, v71, 4, v72
	v_add_u32_e32 v71, 4, v70
	v_xor_b32_e32 v71, v71, v69
	v_lshl_add_u32 v202, v71, 4, v72
	v_add_u32_e32 v71, 8, v70
	v_xor_b32_e32 v71, v71, v69
	v_lshl_add_u32 v203, v71, 4, v72
	v_add_u32_e32 v71, 12, v70
	v_xor_b32_e32 v71, v71, v69
	v_lshl_add_u32 v246, v71, 4, v72
	v_bfe_u32 v73, v69, 1, 3
	v_lshlrev_b32_e32 v76, 7, v69
	v_add_u32_e32 v71, 0, v70
	v_xor_b32_e32 v71, v71, v73
	v_lshl_add_u32 v209, v71, 4, v76
	v_add_u32_e32 v71, 4, v70
	v_xor_b32_e32 v71, v71, v73
	v_lshl_add_u32 v210, v71, 4, v76
	s_lshl_b32 s101, s100, 7
	s_add_u32 s101, s101, 0x8000
	s_cmpk_ge_u32 s100, 0x100
	s_cselect_b32 s6, 0x8000, 0
	s_add_u32 s101, s101, s6
	v_and_b32_e32 v74, 31, v68
	v_lshrrev_b32_e32 v75, 5, v68
	v_lshlrev_b32_e32 v74, 8, v74
	v_lshl_add_u32 v74, v75, 4, v74
	v_add_u32_e32 v74, s101, v74
	v_lshlrev_b32_e32 v75, 8, v69
	v_lshl_add_u32 v75, v70, 4, v75
	v_add_u32_e32 v75, s101, v75
	ds_write_b128 v74, v[96:99] offset:0
	ds_write_b128 v74, v[100:103] offset:32
	ds_write_b128 v74, v[104:107] offset:64
	ds_write_b128 v74, v[108:111] offset:96
	ds_write_b128 v74, v[112:115] offset:128
	ds_write_b128 v74, v[116:119] offset:160
	ds_write_b128 v74, v[120:123] offset:192
	ds_write_b128 v74, v[124:127] offset:224
	s_waitcnt lgkmcnt(0)
	ds_read_b128 v[96:99], v75 offset:0
	ds_read_b128 v[100:103], v75 offset:64
	ds_read_b128 v[104:107], v75 offset:128
	ds_read_b128 v[108:111], v75 offset:192
	ds_read_b128 v[112:115], v75 offset:4096
	ds_read_b128 v[116:119], v75 offset:4160
	ds_read_b128 v[120:123], v75 offset:4224
	ds_read_b128 v[124:127], v75 offset:4288
	s_waitcnt vmcnt(0)
	s_waitcnt lgkmcnt(0)
	s_barrier
	ds_write_b128 v225, v[136:139] offset:32768
	ds_write_b128 v226, v[140:143] offset:32768
	s_add_u32 s15, s22, s12
	s_addc_u32 s14, s23, s13
	s_add_u32 s6, s15, 0x23a40000
	s_addc_u32 s7, s14, 0
	s_waitcnt lgkmcnt(0)
	global_load_dwordx4 v[136:139], v196, s[6:7]
	global_load_dwordx4 v[140:143], v197, s[6:7]
	v_mov_b32_e32 v194, 0
	v_mov_b32_e32 v195, 0
	s_barrier
	s_add_u32 s8, s22, s10
	s_addc_u32 s9, s23, s11
	s_add_u32 s8, s8, 0x3bc00200
	s_addc_u32 s9, s9, 0
	s_and_b32 s101, s0, 0x104
	s_cmpk_ge_u32 s100, 0x100
	s_cselect_b32 s100, 1, 0
	ds_read_b128 v[160:163], v201 offset:0
	ds_read_b128 v[164:167], v202 offset:0
	ds_read_b128 v[168:171], v203 offset:0
	ds_read_b128 v[172:175], v246 offset:0
	ds_read_b128 v[176:179], v201 offset:4096
	ds_read_b128 v[180:183], v202 offset:4096
	ds_read_b128 v[230:233], v203 offset:4096
	s_waitcnt lgkmcnt(6)
	v_mfma_f32_16x16x32_bf16 v[64:67], v[160:163], v[96:99], 0
	v_mfma_f32_16x16x32_bf16 v[68:71], v[160:163], v[112:115], 0
	ds_read_b128 v[234:237], v246 offset:4096
	s_waitcnt lgkmcnt(6)
	v_mfma_f32_16x16x32_bf16 v[68:71], v[164:167], v[116:119], v[68:71]
	v_mfma_f32_16x16x32_bf16 v[64:67], v[164:167], v[100:103], v[64:67]
	ds_read_b128 v[160:163], v201 offset:8192
	s_waitcnt lgkmcnt(6)
	v_mfma_f32_16x16x32_bf16 v[64:67], v[168:171], v[104:107], v[64:67]
	v_mfma_f32_16x16x32_bf16 v[68:71], v[168:171], v[120:123], v[68:71]
	ds_read_b128 v[164:167], v202 offset:8192
	s_waitcnt lgkmcnt(6)
	v_mfma_f32_16x16x32_bf16 v[68:71], v[172:175], v[124:127], v[68:71]
	v_mfma_f32_16x16x32_bf16 v[64:67], v[172:175], v[108:111], v[64:67]
	ds_read_b128 v[168:171], v203 offset:8192
	s_waitcnt lgkmcnt(6)
	v_mfma_f32_16x16x32_bf16 v[72:75], v[176:179], v[96:99], 0
	s_nop 7
	s_nop 1
	v_exp_f32_e32 v64, v64
	v_mfma_f32_16x16x32_bf16 v[76:79], v[176:179], v[112:115], 0
	v_exp_f32_e32 v68, v68
	ds_read_b128 v[172:175], v246 offset:8192
	s_waitcnt lgkmcnt(6)
	v_mfma_f32_16x16x32_bf16 v[76:79], v[180:183], v[116:119], v[76:79]
	v_exp_f32_e32 v65, v65
	v_exp_f32_e32 v69, v69
	v_mfma_f32_16x16x32_bf16 v[72:75], v[180:183], v[100:103], v[72:75]
	v_exp_f32_e32 v66, v66
	ds_read_b128 v[176:179], v201 offset:12288
	s_waitcnt lgkmcnt(6)
	v_mfma_f32_16x16x32_bf16 v[72:75], v[230:233], v[104:107], v[72:75]
	v_exp_f32_e32 v70, v70
	v_exp_f32_e32 v67, v67
	v_mfma_f32_16x16x32_bf16 v[76:79], v[230:233], v[120:123], v[76:79]
	v_exp_f32_e32 v71, v71
	v_add_f32_e32 v220, v64, v65
	ds_read_b128 v[180:183], v202 offset:12288
	s_waitcnt lgkmcnt(6)
	v_mfma_f32_16x16x32_bf16 v[76:79], v[234:237], v[124:127], v[76:79]
	v_add_f32_e32 v221, v68, v69
	v_add_f32_e32 v220, v220, v66
	v_add_f32_e32 v221, v221, v70
	v_mfma_f32_16x16x32_bf16 v[72:75], v[234:237], v[108:111], v[72:75]
	v_add_f32_e32 v220, v220, v67
	v_add_f32_e32 v221, v221, v71
	ds_read_b128 v[230:233], v203 offset:12288
	s_waitcnt lgkmcnt(6)
	v_mfma_f32_16x16x32_bf16 v[80:83], v[160:163], v[96:99], 0
	s_nop 7
	s_nop 1
	v_exp_f32_e32 v72, v72
	v_exp_f32_e32 v76, v76
	v_mfma_f32_16x16x32_bf16 v[84:87], v[160:163], v[112:115], 0
	v_exp_f32_e32 v73, v73
	v_exp_f32_e32 v77, v77
	ds_read_b128 v[234:237], v246 offset:12288
	s_waitcnt lgkmcnt(6)
	v_mfma_f32_16x16x32_bf16 v[84:87], v[164:167], v[116:119], v[84:87]
	v_exp_f32_e32 v74, v74
	v_exp_f32_e32 v78, v78
	v_mfma_f32_16x16x32_bf16 v[80:83], v[164:167], v[100:103], v[80:83]
	v_exp_f32_e32 v75, v75
	v_exp_f32_e32 v79, v79
	s_waitcnt lgkmcnt(5)
	v_mfma_f32_16x16x32_bf16 v[80:83], v[168:171], v[104:107], v[80:83]
	v_add_f32_e32 v220, v220, v72
	v_add_f32_e32 v221, v221, v76
	v_add_f32_e32 v220, v220, v73
	v_add_f32_e32 v221, v221, v77
	v_mfma_f32_16x16x32_bf16 v[84:87], v[168:171], v[120:123], v[84:87]
	v_add_f32_e32 v220, v220, v74
	v_add_f32_e32 v221, v221, v78
	v_add_f32_e32 v220, v220, v75
	v_add_f32_e32 v221, v221, v79
	s_waitcnt lgkmcnt(4)
	v_mfma_f32_16x16x32_bf16 v[84:87], v[172:175], v[124:127], v[84:87]
	v_cvt_pk_bf16_f32 v216, v64, v65
	v_cvt_pk_bf16_f32 v217, v66, v67
	v_cvt_pk_bf16_f32 v238, v68, v69
	v_cvt_pk_bf16_f32 v239, v70, v71
	v_mfma_f32_16x16x32_bf16 v[80:83], v[172:175], v[108:111], v[80:83]
	v_cvt_pk_bf16_f32 v218, v72, v73
	v_cvt_pk_bf16_f32 v219, v74, v75
	v_cvt_pk_bf16_f32 v240, v76, v77
	v_cvt_pk_bf16_f32 v241, v78, v79
	s_waitcnt lgkmcnt(3)
	v_mfma_f32_16x16x32_bf16 v[88:91], v[176:179], v[96:99], 0
	s_nop 7
	s_nop 1
	v_exp_f32_e32 v80, v80
	v_exp_f32_e32 v84, v84
	v_mfma_f32_16x16x32_bf16 v[92:95], v[176:179], v[112:115], 0
	v_exp_f32_e32 v81, v81
	s_waitcnt lgkmcnt(2)
	v_mfma_f32_16x16x32_bf16 v[92:95], v[180:183], v[116:119], v[92:95]
	v_exp_f32_e32 v85, v85
	v_exp_f32_e32 v82, v82
	v_mfma_f32_16x16x32_bf16 v[88:91], v[180:183], v[100:103], v[88:91]
	v_exp_f32_e32 v86, v86
	s_waitcnt lgkmcnt(1)
	v_mfma_f32_16x16x32_bf16 v[88:91], v[230:233], v[104:107], v[88:91]
	v_exp_f32_e32 v83, v83
	v_exp_f32_e32 v87, v87
	v_mfma_f32_16x16x32_bf16 v[92:95], v[230:233], v[120:123], v[92:95]
	v_add_f32_e32 v220, v220, v80
	v_add_f32_e32 v221, v221, v84
	v_add_f32_e32 v220, v220, v81
	s_waitcnt lgkmcnt(0)
	v_mfma_f32_16x16x32_bf16 v[92:95], v[234:237], v[124:127], v[92:95]
	v_add_f32_e32 v221, v221, v85
	v_add_f32_e32 v220, v220, v82
	v_add_f32_e32 v221, v221, v86
	v_mfma_f32_16x16x32_bf16 v[88:91], v[234:237], v[108:111], v[88:91]
	v_add_f32_e32 v220, v220, v83
	v_add_f32_e32 v221, v221, v87
	s_waitcnt lgkmcnt(0)
	s_barrier
	ds_read_b128 v[160:163], v201 offset:16384
	ds_read_b128 v[164:167], v209 offset:0
	ds_read_b128 v[168:171], v202 offset:16384
	ds_read_b128 v[172:175], v209 offset:2048
	ds_read_b128 v[176:179], v203 offset:16384
	ds_read_b128 v[180:183], v209 offset:4096
	ds_read_b128 v[230:233], v246 offset:16384
	ds_read_b128 v[234:237], v209 offset:6144

.Lattn_pa0:
	s_waitcnt lgkmcnt(6)
	v_mfma_f32_16x16x32_bf16 v[64:67], v[160:163], v[96:99], 0
	v_exp_f32_e32 v88, v88
	v_mfma_f32_16x16x32_bf16 v[68:71], v[160:163], v[112:115], 0
	v_exp_f32_e32 v92, v92
	ds_read_b128 v[160:163], v201 offset:20480
	s_add_u32 s15, s22, s12
	s_addc_u32 s14, s23, s13
	s_add_u32 s6, s15, 0x23a50000
	s_addc_u32 s7, s14, 0
	v_mfma_f32_16x16x32_bf16 v[0:3], v[164:167], v[216:219], v[0:3]
	v_cvt_pk_bf16_f32 v242, v80, v81
	v_mfma_f32_16x16x32_bf16 v[4:7], v[164:167], v[238:241], v[4:7]
	v_exp_f32_e32 v89, v89
	ds_read_b128 v[164:167], v209 offset:8192
	s_waitcnt vmcnt(4)
	ds_write_b128 v225, v[152:155] offset:49152
	s_waitcnt lgkmcnt(7)
	v_mfma_f32_16x16x32_bf16 v[68:71], v[168:171], v[116:119], v[68:71]
	v_exp_f32_e32 v93, v93
	v_mfma_f32_16x16x32_bf16 v[64:67], v[168:171], v[100:103], v[64:67]
	v_cvt_pk_bf16_f32 v243, v82, v83
	ds_read_b128 v[168:171], v202 offset:20480
	ds_write_b128 v226, v[156:159] offset:49152
	v_mfma_f32_16x16x32_bf16 v[12:15], v[172:175], v[238:241], v[12:15]
	v_exp_f32_e32 v90, v90
	v_mfma_f32_16x16x32_bf16 v[8:11], v[172:175], v[216:219], v[8:11]
	v_exp_f32_e32 v94, v94
	ds_read_b128 v[172:175], v209 offset:10240
	ds_write_b64 v227, v[132:133] offset:32768
	s_waitcnt lgkmcnt(9)
	v_mfma_f32_16x16x32_bf16 v[64:67], v[176:179], v[104:107], v[64:67]
	v_cvt_pk_bf16_f32 v204, v84, v85
	v_mfma_f32_16x16x32_bf16 v[68:71], v[176:179], v[120:123], v[68:71]
	v_exp_f32_e32 v91, v91
	ds_read_b128 v[176:179], v203 offset:20480
	ds_write_b64 v228, v[134:135] offset:32768
	v_mfma_f32_16x16x32_bf16 v[16:19], v[180:183], v[216:219], v[16:19]
	v_exp_f32_e32 v95, v95
	v_mfma_f32_16x16x32_bf16 v[20:23], v[180:183], v[238:241], v[20:23]
	v_cvt_pk_bf16_f32 v205, v86, v87
	v_add_f32_e32 v220, v220, v88
	ds_read_b128 v[180:183], v209 offset:12288
	ds_write_b64 v229, v[128:129] offset:32768
	s_waitcnt lgkmcnt(11)
	v_mfma_f32_16x16x32_bf16 v[68:71], v[230:233], v[124:127], v[68:71]
	v_add_f32_e32 v221, v221, v92
	v_add_f32_e32 v220, v220, v89
	v_mfma_f32_16x16x32_bf16 v[64:67], v[230:233], v[108:111], v[64:67]
	v_add_f32_e32 v221, v221, v93
	v_cvt_pk_bf16_f32 v244, v88, v89
	ds_read_b128 v[230:233], v246 offset:20480
	ds_write_b64 v184, v[130:131] offset:32768
	v_mfma_f32_16x16x32_bf16 v[28:31], v[234:237], v[238:241], v[28:31]
	v_cvt_pk_bf16_f32 v245, v90, v91
	v_cvt_pk_bf16_f32 v206, v92, v93
	v_mfma_f32_16x16x32_bf16 v[24:27], v[234:237], v[216:219], v[24:27]
	v_cvt_pk_bf16_f32 v207, v94, v95
	ds_read_b128 v[234:237], v209 offset:14336
	global_load_dwordx4 v[132:135], v198, s[8:9]
	s_waitcnt lgkmcnt(12)
	v_mfma_f32_16x16x32_bf16 v[72:75], v[160:163], v[96:99], 0
	v_add_f32_e32 v220, v220, v90
	v_add_f32_e32 v221, v221, v94
	v_mfma_f32_16x16x32_bf16 v[76:79], v[160:163], v[112:115], 0
	v_add_f32_e32 v220, v220, v91
	v_add_f32_e32 v221, v221, v95
	ds_read_b128 v[160:163], v201 offset:24576
	global_load_dwordx4 v[128:131], v199, s[8:9]
	v_mfma_f32_16x16x32_bf16 v[32:35], v[164:167], v[216:219], v[32:35]
	v_add_f32_e32 v194, v194, v220
	v_add_f32_e32 v195, v195, v221
	v_mfma_f32_16x16x32_bf16 v[36:39], v[164:167], v[238:241], v[36:39]
	v_exp_f32_e32 v64, v64
	ds_read_b128 v[164:167], v210 offset:0
	global_load_dwordx4 v[152:155], v196, s[6:7]
	s_waitcnt lgkmcnt(10)
	v_mfma_f32_16x16x32_bf16 v[76:79], v[168:171], v[116:119], v[76:79]
	v_exp_f32_e32 v68, v68
	v_mfma_f32_16x16x32_bf16 v[72:75], v[168:171], v[100:103], v[72:75]
	v_exp_f32_e32 v65, v65
	ds_read_b128 v[168:171], v202 offset:24576
	global_load_dwordx4 v[156:159], v197, s[6:7]
	v_mfma_f32_16x16x32_bf16 v[44:47], v[172:175], v[238:241], v[44:47]
	v_exp_f32_e32 v69, v69
	v_mfma_f32_16x16x32_bf16 v[40:43], v[172:175], v[216:219], v[40:43]
	v_exp_f32_e32 v66, v66
	ds_read_b128 v[172:175], v210 offset:2048
	s_waitcnt lgkmcnt(8)
	v_mfma_f32_16x16x32_bf16 v[72:75], v[176:179], v[104:107], v[72:75]
	v_exp_f32_e32 v70, v70
	v_mfma_f32_16x16x32_bf16 v[76:79], v[176:179], v[120:123], v[76:79]
	v_exp_f32_e32 v67, v67
	ds_read_b128 v[176:179], v203 offset:24576
	v_mfma_f32_16x16x32_bf16 v[48:51], v[180:183], v[216:219], v[48:51]
	v_exp_f32_e32 v71, v71
	v_mfma_f32_16x16x32_bf16 v[52:55], v[180:183], v[238:241], v[52:55]
	v_add_f32_e32 v220, v64, v65
	ds_read_b128 v[180:183], v210 offset:4096
	s_waitcnt lgkmcnt(6)
	v_mfma_f32_16x16x32_bf16 v[76:79], v[230:233], v[124:127], v[76:79]
	v_add_f32_e32 v221, v68, v69
	v_mfma_f32_16x16x32_bf16 v[72:75], v[230:233], v[108:111], v[72:75]
	v_add_f32_e32 v220, v220, v66
	ds_read_b128 v[230:233], v246 offset:24576
	v_mfma_f32_16x16x32_bf16 v[60:63], v[234:237], v[238:241], v[60:63]
	v_add_f32_e32 v221, v221, v70
	v_add_f32_e32 v220, v220, v67
	v_mfma_f32_16x16x32_bf16 v[56:59], v[234:237], v[216:219], v[56:59]
	v_add_f32_e32 v221, v221, v71
	ds_read_b128 v[234:237], v210 offset:6144
	s_waitcnt lgkmcnt(6)
	v_mfma_f32_16x16x32_bf16 v[80:83], v[160:163], v[96:99], 0
	v_exp_f32_e32 v72, v72
	v_mfma_f32_16x16x32_bf16 v[84:87], v[160:163], v[112:115], 0
	v_exp_f32_e32 v76, v76
	ds_read_b128 v[160:163], v201 offset:28672
	v_mfma_f32_16x16x32_bf16 v[0:3], v[164:167], v[242:245], v[0:3]
	v_exp_f32_e32 v73, v73
	v_mfma_f32_16x16x32_bf16 v[4:7], v[164:167], v[204:207], v[4:7]
	v_exp_f32_e32 v77, v77
	ds_read_b128 v[164:167], v210 offset:8192
	s_waitcnt lgkmcnt(6)
	v_mfma_f32_16x16x32_bf16 v[84:87], v[168:171], v[116:119], v[84:87]
	v_exp_f32_e32 v74, v74
	v_mfma_f32_16x16x32_bf16 v[80:83], v[168:171], v[100:103], v[80:83]
	v_exp_f32_e32 v78, v78
	ds_read_b128 v[168:171], v202 offset:28672
	v_mfma_f32_16x16x32_bf16 v[12:15], v[172:175], v[204:207], v[12:15]
	v_exp_f32_e32 v75, v75
	v_mfma_f32_16x16x32_bf16 v[8:11], v[172:175], v[242:245], v[8:11]
	v_exp_f32_e32 v79, v79
	ds_read_b128 v[172:175], v210 offset:10240
	s_waitcnt lgkmcnt(6)
	v_mfma_f32_16x16x32_bf16 v[80:83], v[176:179], v[104:107], v[80:83]
	v_add_f32_e32 v220, v220, v72
	v_add_f32_e32 v221, v221, v76
	v_mfma_f32_16x16x32_bf16 v[84:87], v[176:179], v[120:123], v[84:87]
	v_add_f32_e32 v220, v220, v73
	ds_read_b128 v[176:179], v203 offset:28672
	v_mfma_f32_16x16x32_bf16 v[16:19], v[180:183], v[242:245], v[16:19]
	v_add_f32_e32 v221, v221, v77
	v_add_f32_e32 v220, v220, v74
	v_mfma_f32_16x16x32_bf16 v[20:23], v[180:183], v[204:207], v[20:23]
	v_add_f32_e32 v221, v221, v78
	ds_read_b128 v[180:183], v210 offset:12288
	s_waitcnt lgkmcnt(6)
	v_mfma_f32_16x16x32_bf16 v[84:87], v[230:233], v[124:127], v[84:87]
	v_add_f32_e32 v220, v220, v75
	v_add_f32_e32 v221, v221, v79
	v_mfma_f32_16x16x32_bf16 v[80:83], v[230:233], v[108:111], v[80:83]
	v_cvt_pk_bf16_f32 v216, v64, v65
	ds_read_b128 v[230:233], v246 offset:28672
	v_mfma_f32_16x16x32_bf16 v[28:31], v[234:237], v[204:207], v[28:31]
	v_cvt_pk_bf16_f32 v217, v66, v67
	v_cvt_pk_bf16_f32 v238, v68, v69
	v_mfma_f32_16x16x32_bf16 v[24:27], v[234:237], v[242:245], v[24:27]
	v_cvt_pk_bf16_f32 v239, v70, v71
	ds_read_b128 v[234:237], v210 offset:14336
	s_waitcnt lgkmcnt(6)
	v_mfma_f32_16x16x32_bf16 v[88:91], v[160:163], v[96:99], 0
	v_exp_f32_e32 v80, v80
	v_mfma_f32_16x16x32_bf16 v[92:95], v[160:163], v[112:115], 0
	v_exp_f32_e32 v84, v84
	ds_read_b128 v[160:163], v201 offset:32768
	v_mfma_f32_16x16x32_bf16 v[32:35], v[164:167], v[242:245], v[32:35]
	v_exp_f32_e32 v81, v81
	v_mfma_f32_16x16x32_bf16 v[36:39], v[164:167], v[204:207], v[36:39]
	v_exp_f32_e32 v85, v85
	ds_read_b128 v[164:167], v209 offset:16384
	s_waitcnt lgkmcnt(6)
	v_mfma_f32_16x16x32_bf16 v[92:95], v[168:171], v[116:119], v[92:95]
	v_exp_f32_e32 v82, v82
	v_mfma_f32_16x16x32_bf16 v[88:91], v[168:171], v[100:103], v[88:91]
	v_exp_f32_e32 v86, v86
	ds_read_b128 v[168:171], v202 offset:32768
	v_mfma_f32_16x16x32_bf16 v[44:47], v[172:175], v[204:207], v[44:47]
	v_exp_f32_e32 v83, v83
	v_mfma_f32_16x16x32_bf16 v[40:43], v[172:175], v[242:245], v[40:43]
	v_exp_f32_e32 v87, v87
	ds_read_b128 v[172:175], v209 offset:18432
	s_waitcnt lgkmcnt(6)
	v_mfma_f32_16x16x32_bf16 v[88:91], v[176:179], v[104:107], v[88:91]
	v_add_f32_e32 v220, v220, v80
	v_add_f32_e32 v221, v221, v84
	v_mfma_f32_16x16x32_bf16 v[92:95], v[176:179], v[120:123], v[92:95]
	v_add_f32_e32 v220, v220, v81
	ds_read_b128 v[176:179], v203 offset:32768
	v_mfma_f32_16x16x32_bf16 v[48:51], v[180:183], v[242:245], v[48:51]
	v_add_f32_e32 v221, v221, v85
	v_add_f32_e32 v220, v220, v82
	v_mfma_f32_16x16x32_bf16 v[52:55], v[180:183], v[204:207], v[52:55]
	v_add_f32_e32 v221, v221, v86
	ds_read_b128 v[180:183], v209 offset:20480
	s_waitcnt lgkmcnt(6)
	v_mfma_f32_16x16x32_bf16 v[92:95], v[230:233], v[124:127], v[92:95]
	v_add_f32_e32 v220, v220, v83
	v_add_f32_e32 v221, v221, v87
	v_mfma_f32_16x16x32_bf16 v[88:91], v[230:233], v[108:111], v[88:91]
	v_cvt_pk_bf16_f32 v218, v72, v73
	ds_read_b128 v[230:233], v246 offset:32768
	v_mfma_f32_16x16x32_bf16 v[60:63], v[234:237], v[204:207], v[60:63]
	v_cvt_pk_bf16_f32 v219, v74, v75
	v_cvt_pk_bf16_f32 v240, v76, v77
	v_mfma_f32_16x16x32_bf16 v[56:59], v[234:237], v[242:245], v[56:59]
	v_cvt_pk_bf16_f32 v241, v78, v79
	ds_read_b128 v[234:237], v209 offset:22528
	s_setprio 0
	s_waitcnt lgkmcnt(6)
	v_mfma_f32_16x16x32_bf16 v[64:67], v[160:163], v[96:99], 0
	v_exp_f32_e32 v88, v88
	v_mfma_f32_16x16x32_bf16 v[68:71], v[160:163], v[112:115], 0
	v_exp_f32_e32 v92, v92
	ds_read_b128 v[160:163], v201 offset:36864
	s_add_u32 s6, s15, 0x23a60000
	s_addc_u32 s7, s14, 0
	v_mfma_f32_16x16x32_bf16 v[0:3], v[164:167], v[216:219], v[0:3]
	v_cvt_pk_bf16_f32 v242, v80, v81
	v_mfma_f32_16x16x32_bf16 v[4:7], v[164:167], v[238:241], v[4:7]
	v_exp_f32_e32 v89, v89
	ds_read_b128 v[164:167], v209 offset:24576
	s_waitcnt vmcnt(4)
	ds_write_b128 v225, v[136:139] offset:0
	s_waitcnt lgkmcnt(7)
	v_mfma_f32_16x16x32_bf16 v[68:71], v[168:171], v[116:119], v[68:71]
	v_exp_f32_e32 v93, v93
	v_mfma_f32_16x16x32_bf16 v[64:67], v[168:171], v[100:103], v[64:67]
	v_cvt_pk_bf16_f32 v243, v82, v83
	ds_read_b128 v[168:171], v202 offset:36864
	ds_write_b128 v226, v[140:143] offset:0
	v_mfma_f32_16x16x32_bf16 v[12:15], v[172:175], v[238:241], v[12:15]
	v_exp_f32_e32 v90, v90
	v_mfma_f32_16x16x32_bf16 v[8:11], v[172:175], v[216:219], v[8:11]
	v_exp_f32_e32 v94, v94
	ds_read_b128 v[172:175], v209 offset:26624
	ds_write_b64 v227, v[148:149] offset:49152
	s_waitcnt lgkmcnt(9)
	v_mfma_f32_16x16x32_bf16 v[64:67], v[176:179], v[104:107], v[64:67]
	v_cvt_pk_bf16_f32 v204, v84, v85
	v_mfma_f32_16x16x32_bf16 v[68:71], v[176:179], v[120:123], v[68:71]
	v_exp_f32_e32 v91, v91
	ds_read_b128 v[176:179], v203 offset:36864
	ds_write_b64 v228, v[150:151] offset:49152
	v_mfma_f32_16x16x32_bf16 v[16:19], v[180:183], v[216:219], v[16:19]
	v_exp_f32_e32 v95, v95
	v_mfma_f32_16x16x32_bf16 v[20:23], v[180:183], v[238:241], v[20:23]
	v_cvt_pk_bf16_f32 v205, v86, v87
	v_add_f32_e32 v220, v220, v88
	ds_read_b128 v[180:183], v209 offset:28672
	ds_write_b64 v229, v[144:145] offset:49152
	s_waitcnt lgkmcnt(11)
	v_mfma_f32_16x16x32_bf16 v[68:71], v[230:233], v[124:127], v[68:71]
	v_add_f32_e32 v221, v221, v92
	v_add_f32_e32 v220, v220, v89
	v_mfma_f32_16x16x32_bf16 v[64:67], v[230:233], v[108:111], v[64:67]
	v_add_f32_e32 v221, v221, v93
	v_cvt_pk_bf16_f32 v244, v88, v89
	ds_read_b128 v[230:233], v246 offset:36864
	ds_write_b64 v184, v[146:147] offset:49152
	v_mfma_f32_16x16x32_bf16 v[28:31], v[234:237], v[238:241], v[28:31]
	v_cvt_pk_bf16_f32 v245, v90, v91
	v_cvt_pk_bf16_f32 v206, v92, v93
	v_mfma_f32_16x16x32_bf16 v[24:27], v[234:237], v[216:219], v[24:27]
	v_cvt_pk_bf16_f32 v207, v94, v95
	ds_read_b128 v[234:237], v209 offset:30720
	global_load_dwordx4 v[148:151], v198, s[8:9] offset:128
	s_waitcnt lgkmcnt(12)
	v_mfma_f32_16x16x32_bf16 v[72:75], v[160:163], v[96:99], 0
	v_add_f32_e32 v220, v220, v90
	v_add_f32_e32 v221, v221, v94
	v_mfma_f32_16x16x32_bf16 v[76:79], v[160:163], v[112:115], 0
	v_add_f32_e32 v220, v220, v91
	v_add_f32_e32 v221, v221, v95
	ds_read_b128 v[160:163], v201 offset:40960
	global_load_dwordx4 v[144:147], v199, s[8:9] offset:128
	v_mfma_f32_16x16x32_bf16 v[32:35], v[164:167], v[216:219], v[32:35]
	v_add_f32_e32 v194, v194, v220
	v_add_f32_e32 v195, v195, v221
	v_mfma_f32_16x16x32_bf16 v[36:39], v[164:167], v[238:241], v[36:39]
	v_exp_f32_e32 v64, v64
	ds_read_b128 v[164:167], v210 offset:16384
	global_load_dwordx4 v[136:139], v196, s[6:7]
	s_waitcnt lgkmcnt(10)
	v_mfma_f32_16x16x32_bf16 v[76:79], v[168:171], v[116:119], v[76:79]
	v_exp_f32_e32 v68, v68
	v_mfma_f32_16x16x32_bf16 v[72:75], v[168:171], v[100:103], v[72:75]
	v_exp_f32_e32 v65, v65
	ds_read_b128 v[168:171], v202 offset:40960
	global_load_dwordx4 v[140:143], v197, s[6:7]
	v_mfma_f32_16x16x32_bf16 v[44:47], v[172:175], v[238:241], v[44:47]
	v_exp_f32_e32 v69, v69
	v_mfma_f32_16x16x32_bf16 v[40:43], v[172:175], v[216:219], v[40:43]
	v_exp_f32_e32 v66, v66
	ds_read_b128 v[172:175], v210 offset:18432
	s_waitcnt lgkmcnt(8)
	v_mfma_f32_16x16x32_bf16 v[72:75], v[176:179], v[104:107], v[72:75]
	v_exp_f32_e32 v70, v70
	v_mfma_f32_16x16x32_bf16 v[76:79], v[176:179], v[120:123], v[76:79]
	v_exp_f32_e32 v67, v67
	ds_read_b128 v[176:179], v203 offset:40960
	v_mfma_f32_16x16x32_bf16 v[48:51], v[180:183], v[216:219], v[48:51]
	v_exp_f32_e32 v71, v71
	v_mfma_f32_16x16x32_bf16 v[52:55], v[180:183], v[238:241], v[52:55]
	v_add_f32_e32 v220, v64, v65
	ds_read_b128 v[180:183], v210 offset:20480
	s_waitcnt lgkmcnt(6)
	v_mfma_f32_16x16x32_bf16 v[76:79], v[230:233], v[124:127], v[76:79]
	v_add_f32_e32 v221, v68, v69
	v_mfma_f32_16x16x32_bf16 v[72:75], v[230:233], v[108:111], v[72:75]
	v_add_f32_e32 v220, v220, v66
	ds_read_b128 v[230:233], v246 offset:40960
	v_mfma_f32_16x16x32_bf16 v[60:63], v[234:237], v[238:241], v[60:63]
	v_add_f32_e32 v221, v221, v70
	v_add_f32_e32 v220, v220, v67
	v_mfma_f32_16x16x32_bf16 v[56:59], v[234:237], v[216:219], v[56:59]
	v_add_f32_e32 v221, v221, v71
	ds_read_b128 v[234:237], v210 offset:22528
	s_waitcnt lgkmcnt(6)
	v_mfma_f32_16x16x32_bf16 v[80:83], v[160:163], v[96:99], 0
	v_exp_f32_e32 v72, v72
	v_mfma_f32_16x16x32_bf16 v[84:87], v[160:163], v[112:115], 0
	v_exp_f32_e32 v76, v76
	ds_read_b128 v[160:163], v201 offset:45056
	v_mfma_f32_16x16x32_bf16 v[0:3], v[164:167], v[242:245], v[0:3]
	v_exp_f32_e32 v73, v73
	v_mfma_f32_16x16x32_bf16 v[4:7], v[164:167], v[204:207], v[4:7]
	v_exp_f32_e32 v77, v77
	ds_read_b128 v[164:167], v210 offset:24576
	s_waitcnt lgkmcnt(6)
	v_mfma_f32_16x16x32_bf16 v[84:87], v[168:171], v[116:119], v[84:87]
	v_exp_f32_e32 v74, v74
	v_mfma_f32_16x16x32_bf16 v[80:83], v[168:171], v[100:103], v[80:83]
	v_exp_f32_e32 v78, v78
	ds_read_b128 v[168:171], v202 offset:45056
	v_mfma_f32_16x16x32_bf16 v[12:15], v[172:175], v[204:207], v[12:15]
	v_exp_f32_e32 v75, v75
	v_mfma_f32_16x16x32_bf16 v[8:11], v[172:175], v[242:245], v[8:11]
	v_exp_f32_e32 v79, v79
	ds_read_b128 v[172:175], v210 offset:26624
	s_waitcnt lgkmcnt(6)
	v_mfma_f32_16x16x32_bf16 v[80:83], v[176:179], v[104:107], v[80:83]
	v_add_f32_e32 v220, v220, v72
	v_add_f32_e32 v221, v221, v76
	v_mfma_f32_16x16x32_bf16 v[84:87], v[176:179], v[120:123], v[84:87]
	v_add_f32_e32 v220, v220, v73
	ds_read_b128 v[176:179], v203 offset:45056
	v_mfma_f32_16x16x32_bf16 v[16:19], v[180:183], v[242:245], v[16:19]
	v_add_f32_e32 v221, v221, v77
	v_add_f32_e32 v220, v220, v74
	v_mfma_f32_16x16x32_bf16 v[20:23], v[180:183], v[204:207], v[20:23]
	v_add_f32_e32 v221, v221, v78
	ds_read_b128 v[180:183], v210 offset:28672
	s_waitcnt lgkmcnt(6)
	v_mfma_f32_16x16x32_bf16 v[84:87], v[230:233], v[124:127], v[84:87]
	v_add_f32_e32 v220, v220, v75
	v_add_f32_e32 v221, v221, v79
	v_mfma_f32_16x16x32_bf16 v[80:83], v[230:233], v[108:111], v[80:83]
	v_cvt_pk_bf16_f32 v216, v64, v65
	ds_read_b128 v[230:233], v246 offset:45056
	v_mfma_f32_16x16x32_bf16 v[28:31], v[234:237], v[204:207], v[28:31]
	v_cvt_pk_bf16_f32 v217, v66, v67
	v_cvt_pk_bf16_f32 v238, v68, v69
	v_mfma_f32_16x16x32_bf16 v[24:27], v[234:237], v[242:245], v[24:27]
	v_cvt_pk_bf16_f32 v239, v70, v71
	ds_read_b128 v[234:237], v210 offset:30720
	s_waitcnt lgkmcnt(6)
	v_mfma_f32_16x16x32_bf16 v[88:91], v[160:163], v[96:99], 0
	v_exp_f32_e32 v80, v80
	v_mfma_f32_16x16x32_bf16 v[92:95], v[160:163], v[112:115], 0
	v_exp_f32_e32 v84, v84
	v_mfma_f32_16x16x32_bf16 v[32:35], v[164:167], v[242:245], v[32:35]
	v_exp_f32_e32 v81, v81
	v_mfma_f32_16x16x32_bf16 v[36:39], v[164:167], v[204:207], v[36:39]
	v_exp_f32_e32 v85, v85
	s_waitcnt lgkmcnt(4)
	v_mfma_f32_16x16x32_bf16 v[92:95], v[168:171], v[116:119], v[92:95]
	v_exp_f32_e32 v82, v82
	v_mfma_f32_16x16x32_bf16 v[88:91], v[168:171], v[100:103], v[88:91]
	v_exp_f32_e32 v86, v86
	v_mfma_f32_16x16x32_bf16 v[44:47], v[172:175], v[204:207], v[44:47]
	v_exp_f32_e32 v83, v83
	v_mfma_f32_16x16x32_bf16 v[40:43], v[172:175], v[242:245], v[40:43]
	v_exp_f32_e32 v87, v87
	s_waitcnt lgkmcnt(3)
	v_mfma_f32_16x16x32_bf16 v[88:91], v[176:179], v[104:107], v[88:91]
	v_add_f32_e32 v220, v220, v80
	v_add_f32_e32 v221, v221, v84
	v_mfma_f32_16x16x32_bf16 v[92:95], v[176:179], v[120:123], v[92:95]
	v_add_f32_e32 v220, v220, v81
	s_waitcnt lgkmcnt(0)
	s_barrier
	ds_read_b128 v[160:163], v201 offset:49152
	ds_read_b128 v[164:167], v209 offset:32768
	ds_read_b128 v[168:171], v202 offset:49152
	ds_read_b128 v[172:175], v209 offset:34816
	ds_read_b128 v[176:179], v203 offset:49152
	v_mfma_f32_16x16x32_bf16 v[48:51], v[180:183], v[242:245], v[48:51]
	v_add_f32_e32 v221, v221, v85
	v_add_f32_e32 v220, v220, v82
	v_mfma_f32_16x16x32_bf16 v[52:55], v[180:183], v[204:207], v[52:55]
	v_add_f32_e32 v221, v221, v86
	ds_read_b128 v[180:183], v209 offset:36864
	v_mfma_f32_16x16x32_bf16 v[92:95], v[230:233], v[124:127], v[92:95]
	v_add_f32_e32 v220, v220, v83
	v_add_f32_e32 v221, v221, v87
	v_mfma_f32_16x16x32_bf16 v[88:91], v[230:233], v[108:111], v[88:91]
	v_cvt_pk_bf16_f32 v218, v72, v73
	ds_read_b128 v[230:233], v246 offset:49152
	v_mfma_f32_16x16x32_bf16 v[60:63], v[234:237], v[204:207], v[60:63]
	v_cvt_pk_bf16_f32 v219, v74, v75
	v_cvt_pk_bf16_f32 v240, v76, v77
	v_mfma_f32_16x16x32_bf16 v[56:59], v[234:237], v[242:245], v[56:59]
	v_cvt_pk_bf16_f32 v241, v78, v79
	ds_read_b128 v[234:237], v209 offset:38912
	s_cmp_eq_u32 s100, 0
	s_cbranch_scc1 .Lattn_pa2
	s_setprio 1
.Lattn_pa2:
	s_waitcnt lgkmcnt(6)
	v_mfma_f32_16x16x32_bf16 v[64:67], v[160:163], v[96:99], 0
	v_exp_f32_e32 v88, v88
	v_mfma_f32_16x16x32_bf16 v[68:71], v[160:163], v[112:115], 0
	v_exp_f32_e32 v92, v92
	ds_read_b128 v[160:163], v201 offset:53248
	s_add_u32 s6, s15, 0x23a70000
	s_addc_u32 s7, s14, 0
	v_mfma_f32_16x16x32_bf16 v[0:3], v[164:167], v[216:219], v[0:3]
	v_cvt_pk_bf16_f32 v242, v80, v81
	v_mfma_f32_16x16x32_bf16 v[4:7], v[164:167], v[238:241], v[4:7]
	v_exp_f32_e32 v89, v89
	ds_read_b128 v[164:167], v209 offset:40960
	s_waitcnt vmcnt(4)
	ds_write_b128 v225, v[152:155] offset:16384
	s_waitcnt lgkmcnt(7)
	v_mfma_f32_16x16x32_bf16 v[68:71], v[168:171], v[116:119], v[68:71]
	v_exp_f32_e32 v93, v93
	v_mfma_f32_16x16x32_bf16 v[64:67], v[168:171], v[100:103], v[64:67]
	v_cvt_pk_bf16_f32 v243, v82, v83
	ds_read_b128 v[168:171], v202 offset:53248
	ds_write_b128 v226, v[156:159] offset:16384
	v_mfma_f32_16x16x32_bf16 v[12:15], v[172:175], v[238:241], v[12:15]
	v_exp_f32_e32 v90, v90
	v_mfma_f32_16x16x32_bf16 v[8:11], v[172:175], v[216:219], v[8:11]
	v_exp_f32_e32 v94, v94
	ds_read_b128 v[172:175], v209 offset:43008
	ds_write_b64 v227, v[132:133] offset:0
	s_waitcnt lgkmcnt(9)
	v_mfma_f32_16x16x32_bf16 v[64:67], v[176:179], v[104:107], v[64:67]
	v_cvt_pk_bf16_f32 v204, v84, v85
	v_mfma_f32_16x16x32_bf16 v[68:71], v[176:179], v[120:123], v[68:71]
	v_exp_f32_e32 v91, v91
	ds_read_b128 v[176:179], v203 offset:53248
	ds_write_b64 v228, v[134:135] offset:0
	v_mfma_f32_16x16x32_bf16 v[16:19], v[180:183], v[216:219], v[16:19]
	v_exp_f32_e32 v95, v95
	v_mfma_f32_16x16x32_bf16 v[20:23], v[180:183], v[238:241], v[20:23]
	v_cvt_pk_bf16_f32 v205, v86, v87
	v_add_f32_e32 v220, v220, v88
	ds_read_b128 v[180:183], v209 offset:45056
	ds_write_b64 v229, v[128:129] offset:0
	s_waitcnt lgkmcnt(11)
	v_mfma_f32_16x16x32_bf16 v[68:71], v[230:233], v[124:127], v[68:71]
	v_add_f32_e32 v221, v221, v92
	v_add_f32_e32 v220, v220, v89
	v_mfma_f32_16x16x32_bf16 v[64:67], v[230:233], v[108:111], v[64:67]
	v_add_f32_e32 v221, v221, v93
	v_cvt_pk_bf16_f32 v244, v88, v89
	ds_read_b128 v[230:233], v246 offset:53248
	ds_write_b64 v184, v[130:131] offset:0
	v_mfma_f32_16x16x32_bf16 v[28:31], v[234:237], v[238:241], v[28:31]
	v_cvt_pk_bf16_f32 v245, v90, v91
	v_cvt_pk_bf16_f32 v206, v92, v93
	v_mfma_f32_16x16x32_bf16 v[24:27], v[234:237], v[216:219], v[24:27]
	v_cvt_pk_bf16_f32 v207, v94, v95
	ds_read_b128 v[234:237], v209 offset:47104
	global_load_dwordx4 v[132:135], v198, s[8:9] offset:256
	s_waitcnt lgkmcnt(12)
	v_mfma_f32_16x16x32_bf16 v[72:75], v[160:163], v[96:99], 0
	v_add_f32_e32 v220, v220, v90
	v_add_f32_e32 v221, v221, v94
	v_mfma_f32_16x16x32_bf16 v[76:79], v[160:163], v[112:115], 0
	v_add_f32_e32 v220, v220, v91
	v_add_f32_e32 v221, v221, v95
	ds_read_b128 v[160:163], v201 offset:57344
	global_load_dwordx4 v[128:131], v199, s[8:9] offset:256
	v_mfma_f32_16x16x32_bf16 v[32:35], v[164:167], v[216:219], v[32:35]
	v_add_f32_e32 v194, v194, v220
	v_add_f32_e32 v195, v195, v221
	v_mfma_f32_16x16x32_bf16 v[36:39], v[164:167], v[238:241], v[36:39]
	v_exp_f32_e32 v64, v64
	ds_read_b128 v[164:167], v210 offset:32768
	global_load_dwordx4 v[152:155], v196, s[6:7]
	s_waitcnt lgkmcnt(10)
	v_mfma_f32_16x16x32_bf16 v[76:79], v[168:171], v[116:119], v[76:79]
	v_exp_f32_e32 v68, v68
	v_mfma_f32_16x16x32_bf16 v[72:75], v[168:171], v[100:103], v[72:75]
	v_exp_f32_e32 v65, v65
	ds_read_b128 v[168:171], v202 offset:57344
	global_load_dwordx4 v[156:159], v197, s[6:7]
	v_mfma_f32_16x16x32_bf16 v[44:47], v[172:175], v[238:241], v[44:47]
	v_exp_f32_e32 v69, v69
	v_mfma_f32_16x16x32_bf16 v[40:43], v[172:175], v[216:219], v[40:43]
	v_exp_f32_e32 v66, v66
	ds_read_b128 v[172:175], v210 offset:34816
	s_waitcnt lgkmcnt(8)
	v_mfma_f32_16x16x32_bf16 v[72:75], v[176:179], v[104:107], v[72:75]
	v_exp_f32_e32 v70, v70
	v_mfma_f32_16x16x32_bf16 v[76:79], v[176:179], v[120:123], v[76:79]
	v_exp_f32_e32 v67, v67
	ds_read_b128 v[176:179], v203 offset:57344
	v_mfma_f32_16x16x32_bf16 v[48:51], v[180:183], v[216:219], v[48:51]
	v_exp_f32_e32 v71, v71
	v_mfma_f32_16x16x32_bf16 v[52:55], v[180:183], v[238:241], v[52:55]
	v_add_f32_e32 v220, v64, v65
	ds_read_b128 v[180:183], v210 offset:36864
	s_waitcnt lgkmcnt(6)
	v_mfma_f32_16x16x32_bf16 v[76:79], v[230:233], v[124:127], v[76:79]
	v_add_f32_e32 v221, v68, v69
	v_mfma_f32_16x16x32_bf16 v[72:75], v[230:233], v[108:111], v[72:75]
	v_add_f32_e32 v220, v220, v66
	ds_read_b128 v[230:233], v246 offset:57344
	v_mfma_f32_16x16x32_bf16 v[60:63], v[234:237], v[238:241], v[60:63]
	v_add_f32_e32 v221, v221, v70
	v_add_f32_e32 v220, v220, v67
	v_mfma_f32_16x16x32_bf16 v[56:59], v[234:237], v[216:219], v[56:59]
	v_add_f32_e32 v221, v221, v71
	ds_read_b128 v[234:237], v210 offset:38912
	s_waitcnt lgkmcnt(6)
	v_mfma_f32_16x16x32_bf16 v[80:83], v[160:163], v[96:99], 0
	v_exp_f32_e32 v72, v72
	v_mfma_f32_16x16x32_bf16 v[84:87], v[160:163], v[112:115], 0
	v_exp_f32_e32 v76, v76
	ds_read_b128 v[160:163], v201 offset:61440
	v_mfma_f32_16x16x32_bf16 v[0:3], v[164:167], v[242:245], v[0:3]
	v_exp_f32_e32 v73, v73
	v_mfma_f32_16x16x32_bf16 v[4:7], v[164:167], v[204:207], v[4:7]
	v_exp_f32_e32 v77, v77
	ds_read_b128 v[164:167], v210 offset:40960
	s_waitcnt lgkmcnt(6)
	v_mfma_f32_16x16x32_bf16 v[84:87], v[168:171], v[116:119], v[84:87]
	v_exp_f32_e32 v74, v74
	v_mfma_f32_16x16x32_bf16 v[80:83], v[168:171], v[100:103], v[80:83]
	v_exp_f32_e32 v78, v78
	ds_read_b128 v[168:171], v202 offset:61440
	v_mfma_f32_16x16x32_bf16 v[12:15], v[172:175], v[204:207], v[12:15]
	v_exp_f32_e32 v75, v75
	v_mfma_f32_16x16x32_bf16 v[8:11], v[172:175], v[242:245], v[8:11]
	v_exp_f32_e32 v79, v79
	ds_read_b128 v[172:175], v210 offset:43008
	s_waitcnt lgkmcnt(6)
	v_mfma_f32_16x16x32_bf16 v[80:83], v[176:179], v[104:107], v[80:83]
	v_add_f32_e32 v220, v220, v72
	v_add_f32_e32 v221, v221, v76
	v_mfma_f32_16x16x32_bf16 v[84:87], v[176:179], v[120:123], v[84:87]
	v_add_f32_e32 v220, v220, v73
	ds_read_b128 v[176:179], v203 offset:61440
	v_mfma_f32_16x16x32_bf16 v[16:19], v[180:183], v[242:245], v[16:19]
	v_add_f32_e32 v221, v221, v77
	v_add_f32_e32 v220, v220, v74
	v_mfma_f32_16x16x32_bf16 v[20:23], v[180:183], v[204:207], v[20:23]
	v_add_f32_e32 v221, v221, v78
	ds_read_b128 v[180:183], v210 offset:45056
	s_waitcnt lgkmcnt(6)
	v_mfma_f32_16x16x32_bf16 v[84:87], v[230:233], v[124:127], v[84:87]
	v_add_f32_e32 v220, v220, v75
	v_add_f32_e32 v221, v221, v79
	v_mfma_f32_16x16x32_bf16 v[80:83], v[230:233], v[108:111], v[80:83]
	v_cvt_pk_bf16_f32 v216, v64, v65
	ds_read_b128 v[230:233], v246 offset:61440
	v_mfma_f32_16x16x32_bf16 v[28:31], v[234:237], v[204:207], v[28:31]
	v_cvt_pk_bf16_f32 v217, v66, v67
	v_cvt_pk_bf16_f32 v238, v68, v69
	v_mfma_f32_16x16x32_bf16 v[24:27], v[234:237], v[242:245], v[24:27]
	v_cvt_pk_bf16_f32 v239, v70, v71
	ds_read_b128 v[234:237], v210 offset:47104
	s_waitcnt lgkmcnt(6)
	v_mfma_f32_16x16x32_bf16 v[88:91], v[160:163], v[96:99], 0
	v_exp_f32_e32 v80, v80
	v_mfma_f32_16x16x32_bf16 v[92:95], v[160:163], v[112:115], 0
	v_exp_f32_e32 v84, v84
	ds_read_b128 v[160:163], v201 offset:0
	v_mfma_f32_16x16x32_bf16 v[32:35], v[164:167], v[242:245], v[32:35]
	v_exp_f32_e32 v81, v81
	v_mfma_f32_16x16x32_bf16 v[36:39], v[164:167], v[204:207], v[36:39]
	v_exp_f32_e32 v85, v85
	ds_read_b128 v[164:167], v209 offset:49152
	s_waitcnt lgkmcnt(6)
	v_mfma_f32_16x16x32_bf16 v[92:95], v[168:171], v[116:119], v[92:95]
	v_exp_f32_e32 v82, v82
	v_mfma_f32_16x16x32_bf16 v[88:91], v[168:171], v[100:103], v[88:91]
	v_exp_f32_e32 v86, v86
	ds_read_b128 v[168:171], v202 offset:0
	v_mfma_f32_16x16x32_bf16 v[44:47], v[172:175], v[204:207], v[44:47]
	v_exp_f32_e32 v83, v83
	v_mfma_f32_16x16x32_bf16 v[40:43], v[172:175], v[242:245], v[40:43]
	v_exp_f32_e32 v87, v87
	ds_read_b128 v[172:175], v209 offset:51200
	s_waitcnt lgkmcnt(6)
	v_mfma_f32_16x16x32_bf16 v[88:91], v[176:179], v[104:107], v[88:91]
	v_add_f32_e32 v220, v220, v80
	v_add_f32_e32 v221, v221, v84
	v_mfma_f32_16x16x32_bf16 v[92:95], v[176:179], v[120:123], v[92:95]
	v_add_f32_e32 v220, v220, v81
	ds_read_b128 v[176:179], v203 offset:0
	v_mfma_f32_16x16x32_bf16 v[48:51], v[180:183], v[242:245], v[48:51]
	v_add_f32_e32 v221, v221, v85
	v_add_f32_e32 v220, v220, v82
	v_mfma_f32_16x16x32_bf16 v[52:55], v[180:183], v[204:207], v[52:55]
	v_add_f32_e32 v221, v221, v86
	ds_read_b128 v[180:183], v209 offset:53248
	s_waitcnt lgkmcnt(6)
	v_mfma_f32_16x16x32_bf16 v[92:95], v[230:233], v[124:127], v[92:95]
	v_add_f32_e32 v220, v220, v83
	v_add_f32_e32 v221, v221, v87
	v_mfma_f32_16x16x32_bf16 v[88:91], v[230:233], v[108:111], v[88:91]
	v_cvt_pk_bf16_f32 v218, v72, v73
	ds_read_b128 v[230:233], v246 offset:0
	v_mfma_f32_16x16x32_bf16 v[60:63], v[234:237], v[204:207], v[60:63]
	v_cvt_pk_bf16_f32 v219, v74, v75
	v_cvt_pk_bf16_f32 v240, v76, v77
	v_mfma_f32_16x16x32_bf16 v[56:59], v[234:237], v[242:245], v[56:59]
	v_cvt_pk_bf16_f32 v241, v78, v79
	ds_read_b128 v[234:237], v209 offset:55296
	s_setprio 0
	s_waitcnt lgkmcnt(6)
	v_mfma_f32_16x16x32_bf16 v[64:67], v[160:163], v[96:99], 0
	v_exp_f32_e32 v88, v88
	v_mfma_f32_16x16x32_bf16 v[68:71], v[160:163], v[112:115], 0
	v_exp_f32_e32 v92, v92
	ds_read_b128 v[160:163], v201 offset:4096
	s_add_u32 s6, s15, 0x23a80000
	s_addc_u32 s7, s14, 0
	v_mfma_f32_16x16x32_bf16 v[0:3], v[164:167], v[216:219], v[0:3]
	v_cvt_pk_bf16_f32 v242, v80, v81
	v_mfma_f32_16x16x32_bf16 v[4:7], v[164:167], v[238:241], v[4:7]
	v_exp_f32_e32 v89, v89
	ds_read_b128 v[164:167], v209 offset:57344
	s_waitcnt vmcnt(4)
	ds_write_b128 v225, v[136:139] offset:32768
	s_waitcnt lgkmcnt(7)
	v_mfma_f32_16x16x32_bf16 v[68:71], v[168:171], v[116:119], v[68:71]
	v_exp_f32_e32 v93, v93
	v_mfma_f32_16x16x32_bf16 v[64:67], v[168:171], v[100:103], v[64:67]
	v_cvt_pk_bf16_f32 v243, v82, v83
	ds_read_b128 v[168:171], v202 offset:4096
	ds_write_b128 v226, v[140:143] offset:32768
	v_mfma_f32_16x16x32_bf16 v[12:15], v[172:175], v[238:241], v[12:15]
	v_exp_f32_e32 v90, v90
	v_mfma_f32_16x16x32_bf16 v[8:11], v[172:175], v[216:219], v[8:11]
	v_exp_f32_e32 v94, v94
	ds_read_b128 v[172:175], v209 offset:59392
	ds_write_b64 v227, v[148:149] offset:16384
	s_waitcnt lgkmcnt(9)
	v_mfma_f32_16x16x32_bf16 v[64:67], v[176:179], v[104:107], v[64:67]
	v_cvt_pk_bf16_f32 v204, v84, v85
	v_mfma_f32_16x16x32_bf16 v[68:71], v[176:179], v[120:123], v[68:71]
	v_exp_f32_e32 v91, v91
	ds_read_b128 v[176:179], v203 offset:4096
	ds_write_b64 v228, v[150:151] offset:16384
	v_mfma_f32_16x16x32_bf16 v[16:19], v[180:183], v[216:219], v[16:19]
	v_exp_f32_e32 v95, v95
	v_mfma_f32_16x16x32_bf16 v[20:23], v[180:183], v[238:241], v[20:23]
	v_cvt_pk_bf16_f32 v205, v86, v87
	v_add_f32_e32 v220, v220, v88
	ds_read_b128 v[180:183], v209 offset:61440
	ds_write_b64 v229, v[144:145] offset:16384
	s_waitcnt lgkmcnt(11)
	v_mfma_f32_16x16x32_bf16 v[68:71], v[230:233], v[124:127], v[68:71]
	v_add_f32_e32 v221, v221, v92
	v_add_f32_e32 v220, v220, v89
	v_mfma_f32_16x16x32_bf16 v[64:67], v[230:233], v[108:111], v[64:67]
	v_add_f32_e32 v221, v221, v93
	v_cvt_pk_bf16_f32 v244, v88, v89
	ds_read_b128 v[230:233], v246 offset:4096
	ds_write_b64 v184, v[146:147] offset:16384
	v_mfma_f32_16x16x32_bf16 v[28:31], v[234:237], v[238:241], v[28:31]
	v_cvt_pk_bf16_f32 v245, v90, v91
	v_cvt_pk_bf16_f32 v206, v92, v93
	v_mfma_f32_16x16x32_bf16 v[24:27], v[234:237], v[216:219], v[24:27]
	v_cvt_pk_bf16_f32 v207, v94, v95
	ds_read_b128 v[234:237], v209 offset:63488
	global_load_dwordx4 v[148:151], v198, s[8:9] offset:384
	s_waitcnt lgkmcnt(12)
	v_mfma_f32_16x16x32_bf16 v[72:75], v[160:163], v[96:99], 0
	v_add_f32_e32 v220, v220, v90
	v_add_f32_e32 v221, v221, v94
	v_mfma_f32_16x16x32_bf16 v[76:79], v[160:163], v[112:115], 0
	v_add_f32_e32 v220, v220, v91
	v_add_f32_e32 v221, v221, v95
	ds_read_b128 v[160:163], v201 offset:8192
	global_load_dwordx4 v[144:147], v199, s[8:9] offset:384
	v_mfma_f32_16x16x32_bf16 v[32:35], v[164:167], v[216:219], v[32:35]
	v_add_f32_e32 v194, v194, v220
	v_add_f32_e32 v195, v195, v221
	v_mfma_f32_16x16x32_bf16 v[36:39], v[164:167], v[238:241], v[36:39]
	v_exp_f32_e32 v64, v64
	ds_read_b128 v[164:167], v210 offset:49152
	global_load_dwordx4 v[136:139], v196, s[6:7]
	s_waitcnt lgkmcnt(10)
	v_mfma_f32_16x16x32_bf16 v[76:79], v[168:171], v[116:119], v[76:79]
	v_exp_f32_e32 v68, v68
	v_mfma_f32_16x16x32_bf16 v[72:75], v[168:171], v[100:103], v[72:75]
	v_exp_f32_e32 v65, v65
	ds_read_b128 v[168:171], v202 offset:8192
	global_load_dwordx4 v[140:143], v197, s[6:7]
	v_mfma_f32_16x16x32_bf16 v[44:47], v[172:175], v[238:241], v[44:47]
	v_exp_f32_e32 v69, v69
	v_mfma_f32_16x16x32_bf16 v[40:43], v[172:175], v[216:219], v[40:43]
	v_exp_f32_e32 v66, v66
	ds_read_b128 v[172:175], v210 offset:51200
	s_waitcnt lgkmcnt(8)
	v_mfma_f32_16x16x32_bf16 v[72:75], v[176:179], v[104:107], v[72:75]
	v_exp_f32_e32 v70, v70
	v_mfma_f32_16x16x32_bf16 v[76:79], v[176:179], v[120:123], v[76:79]
	v_exp_f32_e32 v67, v67
	ds_read_b128 v[176:179], v203 offset:8192
	v_mfma_f32_16x16x32_bf16 v[48:51], v[180:183], v[216:219], v[48:51]
	v_exp_f32_e32 v71, v71
	v_mfma_f32_16x16x32_bf16 v[52:55], v[180:183], v[238:241], v[52:55]
	v_add_f32_e32 v220, v64, v65
	ds_read_b128 v[180:183], v210 offset:53248
	s_waitcnt lgkmcnt(6)
	v_mfma_f32_16x16x32_bf16 v[76:79], v[230:233], v[124:127], v[76:79]
	v_add_f32_e32 v221, v68, v69
	v_mfma_f32_16x16x32_bf16 v[72:75], v[230:233], v[108:111], v[72:75]
	v_add_f32_e32 v220, v220, v66
	ds_read_b128 v[230:233], v246 offset:8192
	v_mfma_f32_16x16x32_bf16 v[60:63], v[234:237], v[238:241], v[60:63]
	v_add_f32_e32 v221, v221, v70
	v_add_f32_e32 v220, v220, v67
	v_mfma_f32_16x16x32_bf16 v[56:59], v[234:237], v[216:219], v[56:59]
	v_add_f32_e32 v221, v221, v71
	ds_read_b128 v[234:237], v210 offset:55296
	s_waitcnt lgkmcnt(6)
	v_mfma_f32_16x16x32_bf16 v[80:83], v[160:163], v[96:99], 0
	v_exp_f32_e32 v72, v72
	v_mfma_f32_16x16x32_bf16 v[84:87], v[160:163], v[112:115], 0
	v_exp_f32_e32 v76, v76
	ds_read_b128 v[160:163], v201 offset:12288
	v_mfma_f32_16x16x32_bf16 v[0:3], v[164:167], v[242:245], v[0:3]
	v_exp_f32_e32 v73, v73
	v_mfma_f32_16x16x32_bf16 v[4:7], v[164:167], v[204:207], v[4:7]
	v_exp_f32_e32 v77, v77
	ds_read_b128 v[164:167], v210 offset:57344
	s_waitcnt lgkmcnt(6)
	v_mfma_f32_16x16x32_bf16 v[84:87], v[168:171], v[116:119], v[84:87]
	v_exp_f32_e32 v74, v74
	v_mfma_f32_16x16x32_bf16 v[80:83], v[168:171], v[100:103], v[80:83]
	v_exp_f32_e32 v78, v78
	ds_read_b128 v[168:171], v202 offset:12288
	v_mfma_f32_16x16x32_bf16 v[12:15], v[172:175], v[204:207], v[12:15]
	v_exp_f32_e32 v75, v75
	v_mfma_f32_16x16x32_bf16 v[8:11], v[172:175], v[242:245], v[8:11]
	v_exp_f32_e32 v79, v79
	ds_read_b128 v[172:175], v210 offset:59392
	s_waitcnt lgkmcnt(6)
	v_mfma_f32_16x16x32_bf16 v[80:83], v[176:179], v[104:107], v[80:83]
	v_add_f32_e32 v220, v220, v72
	v_add_f32_e32 v221, v221, v76
	v_mfma_f32_16x16x32_bf16 v[84:87], v[176:179], v[120:123], v[84:87]
	v_add_f32_e32 v220, v220, v73
	ds_read_b128 v[176:179], v203 offset:12288
	s_add_u32 s8, s8, 0x200
	s_addc_u32 s9, s9, 0
	s_add_u32 s12, s12, 0x40000
	s_addc_u32 s13, s13, 0
	s_add_i32 s4, s4, 4
	s_cmp_lt_u32 s4, s101
	s_cselect_b64 vcc, -1, 0
	v_mfma_f32_16x16x32_bf16 v[16:19], v[180:183], v[242:245], v[16:19]
	v_add_f32_e32 v221, v221, v77
	v_add_f32_e32 v220, v220, v74
	v_mfma_f32_16x16x32_bf16 v[20:23], v[180:183], v[204:207], v[20:23]
	v_add_f32_e32 v221, v221, v78
	ds_read_b128 v[180:183], v210 offset:61440
	s_waitcnt lgkmcnt(6)
	v_mfma_f32_16x16x32_bf16 v[84:87], v[230:233], v[124:127], v[84:87]
	v_add_f32_e32 v220, v220, v75
	v_add_f32_e32 v221, v221, v79
	v_mfma_f32_16x16x32_bf16 v[80:83], v[230:233], v[108:111], v[80:83]
	v_cvt_pk_bf16_f32 v216, v64, v65
	ds_read_b128 v[230:233], v246 offset:12288
	v_mfma_f32_16x16x32_bf16 v[28:31], v[234:237], v[204:207], v[28:31]
	v_cvt_pk_bf16_f32 v217, v66, v67
	v_cvt_pk_bf16_f32 v238, v68, v69
	v_mfma_f32_16x16x32_bf16 v[24:27], v[234:237], v[242:245], v[24:27]
	v_cvt_pk_bf16_f32 v239, v70, v71
	ds_read_b128 v[234:237], v210 offset:63488
	s_waitcnt lgkmcnt(6)
	v_mfma_f32_16x16x32_bf16 v[88:91], v[160:163], v[96:99], 0
	v_exp_f32_e32 v80, v80
	v_mfma_f32_16x16x32_bf16 v[92:95], v[160:163], v[112:115], 0
	v_exp_f32_e32 v84, v84
	v_mfma_f32_16x16x32_bf16 v[32:35], v[164:167], v[242:245], v[32:35]
	v_exp_f32_e32 v81, v81
	v_mfma_f32_16x16x32_bf16 v[36:39], v[164:167], v[204:207], v[36:39]
	v_exp_f32_e32 v85, v85
	s_waitcnt lgkmcnt(4)
	v_mfma_f32_16x16x32_bf16 v[92:95], v[168:171], v[116:119], v[92:95]
	v_exp_f32_e32 v82, v82
	v_mfma_f32_16x16x32_bf16 v[88:91], v[168:171], v[100:103], v[88:91]
	v_exp_f32_e32 v86, v86
	v_mfma_f32_16x16x32_bf16 v[44:47], v[172:175], v[204:207], v[44:47]
	v_exp_f32_e32 v83, v83
	v_mfma_f32_16x16x32_bf16 v[40:43], v[172:175], v[242:245], v[40:43]
	v_exp_f32_e32 v87, v87
	s_waitcnt lgkmcnt(3)
	v_mfma_f32_16x16x32_bf16 v[88:91], v[176:179], v[104:107], v[88:91]
	v_add_f32_e32 v220, v220, v80
	v_add_f32_e32 v221, v221, v84
	v_mfma_f32_16x16x32_bf16 v[92:95], v[176:179], v[120:123], v[92:95]
	v_add_f32_e32 v220, v220, v81
	s_waitcnt lgkmcnt(0)
	s_barrier
	ds_read_b128 v[160:163], v201 offset:16384
	ds_read_b128 v[164:167], v209 offset:0
	ds_read_b128 v[168:171], v202 offset:16384
	ds_read_b128 v[172:175], v209 offset:2048
	ds_read_b128 v[176:179], v203 offset:16384
	v_mfma_f32_16x16x32_bf16 v[48:51], v[180:183], v[242:245], v[48:51]
	v_add_f32_e32 v221, v221, v85
	v_add_f32_e32 v220, v220, v82
	v_mfma_f32_16x16x32_bf16 v[52:55], v[180:183], v[204:207], v[52:55]
	v_add_f32_e32 v221, v221, v86
	ds_read_b128 v[180:183], v209 offset:4096
	v_mfma_f32_16x16x32_bf16 v[92:95], v[230:233], v[124:127], v[92:95]
	v_add_f32_e32 v220, v220, v83
	v_add_f32_e32 v221, v221, v87
	v_mfma_f32_16x16x32_bf16 v[88:91], v[230:233], v[108:111], v[88:91]
	v_cvt_pk_bf16_f32 v218, v72, v73
	ds_read_b128 v[230:233], v246 offset:16384
	v_mfma_f32_16x16x32_bf16 v[60:63], v[234:237], v[204:207], v[60:63]
	v_cvt_pk_bf16_f32 v219, v74, v75
	v_cvt_pk_bf16_f32 v240, v76, v77
	v_mfma_f32_16x16x32_bf16 v[56:59], v[234:237], v[242:245], v[56:59]
	v_cvt_pk_bf16_f32 v241, v78, v79
	ds_read_b128 v[234:237], v209 offset:6144
	s_cbranch_vccnz .LBB0_734
	s_setprio 0
	s_waitcnt vmcnt(0)
	s_nop 7
	s_nop 7
	ds_swizzle_b32 v64, v194 offset:swizzle(SWAP,16)
	s_waitcnt lgkmcnt(0)
	v_add_f32_e32 v194, v194, v64
	v_mov_b32_e32 v65, v194
	s_nop 1
	v_permlane32_swap_b32_e32 v194, v65
	v_add_f32_e32 v194, v194, v65
	s_nop 0
	v_rcp_f32_e32 v66, v194
	ds_swizzle_b32 v64, v195 offset:swizzle(SWAP,16)
	s_waitcnt lgkmcnt(0)
	v_add_f32_e32 v195, v195, v64
	v_mov_b32_e32 v65, v195
	s_nop 1
	v_permlane32_swap_b32_e32 v195, v65
	v_add_f32_e32 v195, v195, v65
	s_nop 0
	v_rcp_f32_e32 v67, v195
	v_readlane_b32 s100, v250, 8
	v_mbcnt_lo_u32_b32 v68, -1, 0
	v_mbcnt_hi_u32_b32 v68, -1, v68
	v_and_b32_e32 v69, 15, v68
	v_lshrrev_b32_e32 v70, 4, v68
	s_lshr_b32 s101, s100, 1
	v_add_u32_e32 v69, s101, v69
	v_lshlrev_b32_e32 v69, 12, v69
	v_and_b32_e32 v71, 1, v70
	v_lshlrev_b32_e32 v71, 5, v71
	v_and_b32_e32 v70, 2, v70
	v_lshl_add_u32 v71, v70, 3, v71
	v_add_u32_e32 v70, v69, v71
	v_add_u32_e32 v71, 0x10000, v70
	v_mul_f32_e32 v0, v0, v66
	v_mul_f32_e32 v1, v1, v66
	v_mul_f32_e32 v2, v2, v66
	v_mul_f32_e32 v3, v3, v66
	v_mul_f32_e32 v8, v8, v66
	v_mul_f32_e32 v9, v9, v66
	v_mul_f32_e32 v10, v10, v66
	v_mul_f32_e32 v11, v11, v66
	v_cvt_pk_bf16_f32 v72, v0, v1
	v_cvt_pk_bf16_f32 v73, v2, v3
	v_cvt_pk_bf16_f32 v74, v8, v9
	v_cvt_pk_bf16_f32 v75, v10, v11
	s_nop 1
	v_permlane16_swap_b32_e32 v72, v74
	v_permlane16_swap_b32_e32 v73, v75
	s_nop 1
	global_store_dwordx4 v70, v[72:75], s[58:59] offset:0
	v_mul_f32_e32 v16, v16, v66
	v_mul_f32_e32 v17, v17, v66
	v_mul_f32_e32 v18, v18, v66
	v_mul_f32_e32 v19, v19, v66
	v_mul_f32_e32 v24, v24, v66
	v_mul_f32_e32 v25, v25, v66
	v_mul_f32_e32 v26, v26, v66
	v_mul_f32_e32 v27, v27, v66
	v_cvt_pk_bf16_f32 v76, v16, v17
	v_cvt_pk_bf16_f32 v77, v18, v19
	v_cvt_pk_bf16_f32 v78, v24, v25
	v_cvt_pk_bf16_f32 v79, v26, v27
	s_nop 1
	v_permlane16_swap_b32_e32 v76, v78
	v_permlane16_swap_b32_e32 v77, v79
	s_nop 1
	global_store_dwordx4 v70, v[76:79], s[58:59] offset:64
	v_mul_f32_e32 v32, v32, v66
	v_mul_f32_e32 v33, v33, v66
	v_mul_f32_e32 v34, v34, v66
	v_mul_f32_e32 v35, v35, v66
	v_mul_f32_e32 v40, v40, v66
	v_mul_f32_e32 v41, v41, v66
	v_mul_f32_e32 v42, v42, v66
	v_mul_f32_e32 v43, v43, v66
	v_cvt_pk_bf16_f32 v80, v32, v33
	v_cvt_pk_bf16_f32 v81, v34, v35
	v_cvt_pk_bf16_f32 v82, v40, v41
	v_cvt_pk_bf16_f32 v83, v42, v43
	s_nop 1
	v_permlane16_swap_b32_e32 v80, v82
	v_permlane16_swap_b32_e32 v81, v83
	s_nop 1
	global_store_dwordx4 v70, v[80:83], s[58:59] offset:128
	v_mul_f32_e32 v48, v48, v66
	v_mul_f32_e32 v49, v49, v66
	v_mul_f32_e32 v50, v50, v66
	v_mul_f32_e32 v51, v51, v66
	v_mul_f32_e32 v56, v56, v66
	v_mul_f32_e32 v57, v57, v66
	v_mul_f32_e32 v58, v58, v66
	v_mul_f32_e32 v59, v59, v66
	v_cvt_pk_bf16_f32 v84, v48, v49
	v_cvt_pk_bf16_f32 v85, v50, v51
	v_cvt_pk_bf16_f32 v86, v56, v57
	v_cvt_pk_bf16_f32 v87, v58, v59
	s_nop 1
	v_permlane16_swap_b32_e32 v84, v86
	v_permlane16_swap_b32_e32 v85, v87
	s_nop 1
	global_store_dwordx4 v70, v[84:87], s[58:59] offset:192
	v_mul_f32_e32 v4, v4, v67
	v_mul_f32_e32 v5, v5, v67
	v_mul_f32_e32 v6, v6, v67
	v_mul_f32_e32 v7, v7, v67
	v_mul_f32_e32 v12, v12, v67
	v_mul_f32_e32 v13, v13, v67
	v_mul_f32_e32 v14, v14, v67
	v_mul_f32_e32 v15, v15, v67
	v_cvt_pk_bf16_f32 v88, v4, v5
	v_cvt_pk_bf16_f32 v89, v6, v7
	v_cvt_pk_bf16_f32 v90, v12, v13
	v_cvt_pk_bf16_f32 v91, v14, v15
	s_nop 1
	v_permlane16_swap_b32_e32 v88, v90
	v_permlane16_swap_b32_e32 v89, v91
	s_nop 1
	global_store_dwordx4 v71, v[88:91], s[58:59] offset:0
	v_mul_f32_e32 v20, v20, v67
	v_mul_f32_e32 v21, v21, v67
	v_mul_f32_e32 v22, v22, v67
	v_mul_f32_e32 v23, v23, v67
	v_mul_f32_e32 v28, v28, v67
	v_mul_f32_e32 v29, v29, v67
	v_mul_f32_e32 v30, v30, v67
	v_mul_f32_e32 v31, v31, v67
	v_cvt_pk_bf16_f32 v92, v20, v21
	v_cvt_pk_bf16_f32 v93, v22, v23
	v_cvt_pk_bf16_f32 v94, v28, v29
	v_cvt_pk_bf16_f32 v95, v30, v31
	s_nop 1
	v_permlane16_swap_b32_e32 v92, v94
	v_permlane16_swap_b32_e32 v93, v95
	s_nop 1
	global_store_dwordx4 v71, v[92:95], s[58:59] offset:64
	v_mul_f32_e32 v36, v36, v67
	v_mul_f32_e32 v37, v37, v67
	v_mul_f32_e32 v38, v38, v67
	v_mul_f32_e32 v39, v39, v67
	v_mul_f32_e32 v44, v44, v67
	v_mul_f32_e32 v45, v45, v67
	v_mul_f32_e32 v46, v46, v67
	v_mul_f32_e32 v47, v47, v67
	v_cvt_pk_bf16_f32 v72, v36, v37
	v_cvt_pk_bf16_f32 v73, v38, v39
	v_cvt_pk_bf16_f32 v74, v44, v45
	v_cvt_pk_bf16_f32 v75, v46, v47
	s_nop 1
	v_permlane16_swap_b32_e32 v72, v74
	v_permlane16_swap_b32_e32 v73, v75
	s_nop 1
	global_store_dwordx4 v71, v[72:75], s[58:59] offset:128
	v_mul_f32_e32 v52, v52, v67
	v_mul_f32_e32 v53, v53, v67
	v_mul_f32_e32 v54, v54, v67
	v_mul_f32_e32 v55, v55, v67
	v_mul_f32_e32 v60, v60, v67
	v_mul_f32_e32 v61, v61, v67
	v_mul_f32_e32 v62, v62, v67
	v_mul_f32_e32 v63, v63, v67
	v_cvt_pk_bf16_f32 v76, v52, v53
	v_cvt_pk_bf16_f32 v77, v54, v55
	v_cvt_pk_bf16_f32 v78, v60, v61
	v_cvt_pk_bf16_f32 v79, v62, v63
	s_nop 1
	v_permlane16_swap_b32_e32 v76, v78
	v_permlane16_swap_b32_e32 v77, v79
	s_nop 1
	global_store_dwordx4 v71, v[76:79], s[58:59] offset:192
	s_barrier
